# lru prep local scan: all LDS reads issued before the dependent chain (on top of the previous combined version)
# speedup vs baseline: 1.0087x; 1.0006x over previous
.LBB0_370:
	v_ashrrev_i32_e32 v11, 6, v30
	v_add_u32_e32 v8, v111, v104
	s_waitcnt lgkmcnt(0)
	s_barrier
	v_lshl_add_u32 v22, v11, 8, v8
	ds_read2st64_b32 v[112:113], v22 offset1:1
	ds_read2st64_b32 v[114:115], v22 offset0:2 offset1:3
	ds_read2st64_b32 v[116:117], v22 offset0:8 offset1:9
	ds_read2st64_b32 v[118:119], v22 offset0:10 offset1:11
	ds_read2st64_b32 v[120:121], v22 offset0:16 offset1:17
	ds_read2st64_b32 v[122:123], v22 offset0:18 offset1:19
	ds_read2st64_b32 v[124:125], v22 offset0:24 offset1:25
	ds_read2st64_b32 v[126:127], v22 offset0:26 offset1:27
	ds_read2st64_b32 v[128:129], v22 offset0:32 offset1:33
	ds_read2st64_b32 v[130:131], v22 offset0:34 offset1:35
	ds_read2st64_b32 v[132:133], v22 offset0:40 offset1:41
	ds_read2st64_b32 v[134:135], v22 offset0:42 offset1:43
	ds_read2st64_b32 v[136:137], v22 offset0:48 offset1:49
	ds_read2st64_b32 v[138:139], v22 offset0:50 offset1:51
	ds_read2st64_b32 v[140:141], v22 offset0:56 offset1:57
	ds_read2st64_b32 v[142:143], v22 offset0:58 offset1:59
	v_lshlrev_b32_e32 v9, 1, v31
	s_movk_i32 s0, 0x104
	v_sub_u32_e32 v10, v8, v9
	v_mad_u64_u32 v[8:9], s[0:1], v11, s0, v[8:9]
	s_waitcnt vmcnt(12) lgkmcnt(0)
	v_fma_f32 v23, v15, v112, v14
	v_fmac_f32_e32 v23, v21, v113
	v_mad_u64_u32 v[10:11], s[0:1], v11, s39, v[10:11]
	s_or_b32 s0, s24, s71
	s_ashr_i32 s1, s0, 31
	v_fmac_f32_e32 v23, v12, v114
	v_fmac_f32_e32 v23, v13, v115
	ds_write_b32 v8, v23 offset:17408
	v_bfe_u32 v9, v23, 16, 1
	v_add3_u32 v9, v23, v9, s25
	ds_write_b16_d16_hi v10, v9 offset:34304
	s_lshl_b64 s[0:1], s[0:1], 13
	v_fma_f32 v9, v15, v116, v14
	v_fmac_f32_e32 v9, v21, v117
	s_add_u32 s2, s69, s0
	s_addc_u32 s3, s70, s1
	v_and_b32_e32 v24, 48, v30
	v_mov_b32_e32 v25, v105
	v_fmac_f32_e32 v9, v12, v118
	v_fmac_f32_e32 v9, v13, v119
	ds_write_b32 v8, v9 offset:19488
	v_bfe_u32 v11, v9, 16, 1
	v_add3_u32 v9, v9, v11, s25
	ds_write_b16_d16_hi v10, v9 offset:35456
	s_or_b32 s0, s24, s72
	v_fma_f32 v9, v15, v120, v14
	v_fmac_f32_e32 v9, v21, v121
	s_ashr_i32 s1, s0, 31
	s_lshl_b64 s[0:1], s[0:1], 13
	s_add_u32 s0, s69, s0
	s_addc_u32 s1, s70, s1
	v_fmac_f32_e32 v9, v12, v122
	v_fmac_f32_e32 v9, v13, v123
	ds_write_b32 v8, v9 offset:21568
	v_bfe_u32 v11, v9, 16, 1
	v_add3_u32 v9, v9, v11, s25
	ds_write_b16_d16_hi v10, v9 offset:36608
	s_mov_b32 s14, 0xbfb8aa3b
	v_fma_f32 v9, v15, v124, v14
	v_fmac_f32_e32 v9, v21, v125
	v_or_b32_e32 v47, 16, v35
	v_cmp_gt_u32_e32 vcc, s21, v30
	v_mov_b32_e32 v67, 1.0
	v_mov_b32_e32 v68, 0
	v_fmac_f32_e32 v9, v12, v126
	v_fmac_f32_e32 v9, v13, v127
	ds_write_b32 v8, v9 offset:23648
	v_bfe_u32 v11, v9, 16, 1
	v_add3_u32 v9, v9, v11, s25
	ds_write_b16_d16_hi v10, v9 offset:37760
	v_fma_f32 v9, v15, v128, v14
	v_fmac_f32_e32 v9, v21, v129
	v_fmac_f32_e32 v9, v12, v130
	v_fmac_f32_e32 v9, v13, v131
	ds_write_b32 v8, v9 offset:25728
	v_bfe_u32 v11, v9, 16, 1
	v_add3_u32 v9, v9, v11, s25
	ds_write_b16_d16_hi v10, v9 offset:38912
	v_fma_f32 v9, v15, v132, v14
	v_fmac_f32_e32 v9, v21, v133
	v_fmac_f32_e32 v9, v12, v134
	v_fmac_f32_e32 v9, v13, v135
	ds_write_b32 v8, v9 offset:27808
	v_bfe_u32 v11, v9, 16, 1
	v_add3_u32 v9, v9, v11, s25
	ds_write_b16_d16_hi v10, v9 offset:40064
	v_fma_f32 v9, v15, v136, v14
	v_fmac_f32_e32 v9, v21, v137
	v_fmac_f32_e32 v9, v12, v138
	v_fmac_f32_e32 v9, v13, v139
	ds_write_b32 v8, v9 offset:29888
	v_bfe_u32 v11, v9, 16, 1
	v_add3_u32 v9, v9, v11, s25
	ds_write_b16_d16_hi v10, v9 offset:41216
	v_fmac_f32_e32 v14, v15, v140
	v_fmac_f32_e32 v14, v21, v141
	v_fmac_f32_e32 v14, v12, v142
	v_fmac_f32_e32 v14, v13, v143
	ds_write_b32 v8, v14 offset:31968
	v_bfe_u32 v8, v14, 16, 1
	v_add3_u32 v8, v14, v8, s25
	v_lshrrev_b32_e32 v16, 2, v30
	ds_write_b16_d16_hi v10, v8 offset:42368
	v_or_b32_e32 v8, s34, v35
	v_and_or_b32 v21, v16, 12, s34
	v_lshlrev_b32_e32 v16, 7, v35
	v_mov_b32_e32 v17, v105
	v_mul_u32_u24_e32 v8, 0x90, v8
	v_lshl_add_u64 v[22:23], s[2:3], 0, v[16:17]
	s_waitcnt lgkmcnt(0)
	s_barrier
	v_add3_u32 v8, v111, v8, v24
	v_lshl_add_u64 v[22:23], v[22:23], 0, v[24:25]
	ds_read_b128 v[12:15], v8 offset:34304
	ds_read_b128 v[8:11], v8 offset:34368
	global_load_dwordx4 v[36:39], v[22:23], off
	global_load_dwordx4 v[48:51], v[22:23], off offset:64
	v_lshl_add_u64 v[16:17], s[0:1], 0, v[16:17]
	v_lshl_add_u64 v[16:17], v[16:17], 0, v[24:25]
	v_lshlrev_b32_e32 v42, 6, v21
	s_waitcnt vmcnt(1) lgkmcnt(1)
	v_mfma_f32_16x16x32_bf16 v[36:39], v[12:15], v[36:39], 0
	global_load_dwordx4 v[52:55], v[16:17], off offset:64
	s_waitcnt vmcnt(1) lgkmcnt(0)
	v_mfma_f32_16x16x32_bf16 v[48:51], v[8:11], v[48:51], v[36:39]
	s_nop 4
	global_load_dwordx4 v[36:39], v[16:17], off
	v_mul_f32_e64 v17, |v20|, s14
	s_nop 0
	v_add_f32_e32 v22, v18, v48
	v_mul_f32_e32 v22, 0xbfb8aa3b, v22
	v_exp_f32_e32 v17, v17
	v_exp_f32_e32 v22, v22
	v_max_f32_e64 v16, -v20, -v20
	v_max_f32_e32 v16, 0, v16
	v_add_f32_e32 v17, 1.0, v17
	v_add_f32_e32 v22, 1.0, v22
	v_log_f32_e32 v17, v17
	v_rcp_f32_e32 v22, v22
	v_or_b32_e32 v20, s73, v35
	v_lshlrev_b32_e32 v48, 7, v47
	v_fmac_f32_e32 v16, 0x3f317218, v17
	v_mul_f32_e32 v22, 0xc1000000, v22
	v_mul_f32_e32 v22, v16, v22
	v_mul_f32_e32 v22, 0x3fb8aa3b, v22
	v_exp_f32_e32 v22, v22
	v_lshlrev_b32_e32 v17, 2, v35
	s_waitcnt vmcnt(0)
	v_mfma_f32_16x16x32_bf16 v[36:39], v[12:15], v[36:39], 0
	v_mfma_f32_16x16x32_bf16 v[52:55], v[8:11], v[52:55], v[36:39]
	s_nop 6
	v_fma_f32 v36, -v22, v22, 1.0
	v_max_f32_e32 v36, 0, v36
	v_add_f32_e32 v23, v19, v52
	v_mul_f32_e32 v23, 0xbfb8aa3b, v23
	v_exp_f32_e32 v23, v23
	v_sqrt_f32_e32 v36, v36
	v_or_b32_e32 v39, 64, v42
	v_or_b32_e32 v38, 0x80, v42
	v_add_f32_e32 v23, 1.0, v23
	v_rcp_f32_e32 v23, v23
	v_or_b32_e32 v37, 0xc0, v42
	v_mul_f32_e32 v23, v23, v36
	v_mul_u32_u24_e32 v36, 0x104, v21
	v_add3_u32 v36, v111, v17, v36
	ds_read_b32 v144, v36 offset:17408
	ds_read_b32 v145, v36 offset:17668
	ds_read_b32 v146, v36 offset:17928
	ds_read_b32 v147, v36 offset:18188
	ds_read_b32 v148, v36 offset:17472
	ds_read_b32 v149, v36 offset:17732
	ds_read_b32 v150, v36 offset:17992
	ds_read_b32 v151, v36 offset:18252
	ds_read_b32 v152, v36 offset:17536
	ds_read_b32 v153, v36 offset:17796
	ds_read_b32 v154, v36 offset:18056
	ds_read_b32 v155, v36 offset:18316
	ds_read_b32 v156, v36 offset:17600
	ds_read_b32 v157, v36 offset:17860
	ds_read_b32 v158, v36 offset:18120
	ds_read_b32 v159, v36 offset:18380
	v_or_b32_e32 v21, v42, v20
	v_lshlrev_b32_e32 v21, 2, v21
	s_waitcnt lgkmcnt(0)
	v_mul_f32_e32 v17, v144, v23
	v_add_u32_e32 v23, v111, v21
	v_add_u32_e32 v21, v28, v21
	ds_write_b32 v23, v22 offset:43520
	ds_write_b32 v21, v17
	v_add_f32_e32 v17, v18, v49
	v_mul_f32_e32 v17, 0xbfb8aa3b, v17
	v_exp_f32_e32 v17, v17
	v_add_f32_e32 v21, v19, v53
	v_mul_f32_e32 v21, 0xbfb8aa3b, v21
	v_exp_f32_e32 v21, v21
	v_add_f32_e32 v17, 1.0, v17
	v_rcp_f32_e32 v17, v17
	v_mov_b32_e32 v49, v105
	v_add_f32_e32 v21, 1.0, v21
	v_rcp_f32_e32 v21, v21
	v_mul_f32_e32 v17, 0xc1000000, v17
	v_mul_f32_e32 v17, v16, v17
	v_mul_f32_e32 v17, 0x3fb8aa3b, v17
	v_exp_f32_e32 v17, v17
	s_nop 0
	v_fma_f32 v22, -v17, v17, 1.0
	v_max_f32_e32 v22, 0, v22
	v_sqrt_f32_e32 v22, v22
	s_nop 0
	v_mul_f32_e32 v21, v21, v22
	v_mul_f32_e32 v21, v145, v21
	v_or_b32_e32 v22, v39, v20
	v_lshlrev_b32_e32 v22, 2, v22
	v_add_u32_e32 v23, v111, v22
	ds_write_b32 v23, v17 offset:43520
	v_add_u32_e32 v17, v28, v22
	ds_write_b32 v17, v21
	v_add_f32_e32 v17, v18, v50
	v_mul_f32_e32 v17, 0xbfb8aa3b, v17
	v_exp_f32_e32 v17, v17
	v_add_f32_e32 v21, v19, v54
	v_mul_f32_e32 v21, 0xbfb8aa3b, v21
	v_exp_f32_e32 v21, v21
	v_add_f32_e32 v17, 1.0, v17
	v_rcp_f32_e32 v17, v17
	v_add_f32_e32 v21, 1.0, v21
	v_rcp_f32_e32 v21, v21
	v_mul_f32_e32 v17, 0xc1000000, v17
	v_mul_f32_e32 v17, v16, v17
	v_mul_f32_e32 v17, 0x3fb8aa3b, v17
	v_exp_f32_e32 v17, v17
	s_nop 0
	v_fma_f32 v22, -v17, v17, 1.0
	v_max_f32_e32 v22, 0, v22
	v_sqrt_f32_e32 v22, v22
	s_nop 0
	v_mul_f32_e32 v21, v21, v22
	v_mul_f32_e32 v21, v146, v21
	v_or_b32_e32 v22, v38, v20
	v_lshlrev_b32_e32 v22, 2, v22
	v_add_u32_e32 v23, v111, v22
	ds_write_b32 v23, v17 offset:43520
	v_add_u32_e32 v17, v28, v22
	ds_write_b32 v17, v21
	v_add_f32_e32 v17, v18, v51
	v_mul_f32_e32 v17, 0xbfb8aa3b, v17
	v_exp_f32_e32 v17, v17
	v_add_f32_e32 v18, v19, v55
	v_mul_f32_e32 v18, 0xbfb8aa3b, v18
	v_exp_f32_e32 v18, v18
	v_add_f32_e32 v17, 1.0, v17
	v_rcp_f32_e32 v17, v17
	v_add_f32_e32 v18, 1.0, v18
	v_rcp_f32_e32 v18, v18
	v_mul_f32_e32 v17, 0xc1000000, v17
	v_mul_f32_e32 v16, v16, v17
	v_mul_f32_e32 v16, 0x3fb8aa3b, v16
	v_exp_f32_e32 v16, v16
	s_nop 0
	v_fma_f32 v17, -v16, v16, 1.0
	v_max_f32_e32 v17, 0, v17
	v_sqrt_f32_e32 v17, v17
	s_nop 0
	v_mul_f32_e32 v17, v18, v17
	v_mul_f32_e32 v17, v147, v17
	v_or_b32_e32 v18, v37, v20
	v_lshlrev_b32_e32 v18, 2, v18
	v_add_u32_e32 v19, v111, v18
	ds_write_b32 v19, v16 offset:43520
	v_add_u32_e32 v16, v28, v18
	ds_write_b32 v16, v17
	v_lshl_add_u64 v[16:17], s[2:3], 0, v[48:49]
	v_lshl_add_u64 v[20:21], v[16:17], 0, v[24:25]
	global_load_dwordx4 v[16:19], v[20:21], off
	s_waitcnt vmcnt(0)
	v_mfma_f32_16x16x32_bf16 v[16:19], v[12:15], v[16:19], 0
	global_load_dwordx4 v[20:23], v[20:21], off offset:64
	s_waitcnt vmcnt(0)
	v_mfma_f32_16x16x32_bf16 v[16:19], v[8:11], v[20:23], v[16:19]
	v_lshl_add_u64 v[20:21], s[0:1], 0, v[48:49]
	v_lshl_add_u64 v[48:49], v[20:21], 0, v[24:25]
	global_load_dwordx4 v[20:23], v[48:49], off
	s_waitcnt vmcnt(0)
	v_mfma_f32_16x16x32_bf16 v[20:23], v[12:15], v[20:23], 0
	global_load_dwordx4 v[48:51], v[48:49], off offset:64
	s_nop 1
	v_add_f32_e32 v16, v45, v16
	v_mul_f32_e32 v16, 0xbfb8aa3b, v16
	s_waitcnt vmcnt(0)
	v_mfma_f32_16x16x32_bf16 v[20:23], v[8:11], v[48:51], v[20:23]
	v_max_f32_e64 v48, -v46, -v46
	v_mul_f32_e64 v46, |v46|, s14
	v_exp_f32_e32 v46, v46
	v_exp_f32_e32 v16, v16
	v_max_f32_e32 v49, 0, v48
	s_nop 2
	v_add_f32_e32 v20, v44, v20
	v_add_f32_e32 v46, 1.0, v46
	v_add_f32_e32 v16, 1.0, v16
	v_log_f32_e32 v46, v46
	v_rcp_f32_e32 v16, v16
	v_mul_f32_e32 v20, 0xbfb8aa3b, v20
	v_exp_f32_e32 v20, v20
	v_fmac_f32_e32 v49, 0x3f317218, v46
	v_mul_f32_e32 v16, 0xc1000000, v16
	v_mul_f32_e32 v16, v49, v16
	v_mul_f32_e32 v16, 0x3fb8aa3b, v16
	v_exp_f32_e32 v16, v16
	v_add_f32_e32 v20, 1.0, v20
	v_rcp_f32_e32 v20, v20
	v_add_u32_e32 v51, s73, v35
	v_fma_f32 v46, -v16, v16, 1.0
	v_max_f32_e32 v46, 0, v46
	v_sqrt_f32_e32 v46, v46
	v_or_b32_e32 v50, s73, v47
	v_add_u32_e32 v47, v42, v51
	v_lshl_add_u32 v48, v47, 2, v111
	v_mul_f32_e32 v20, v20, v46
	ds_write_b32 v48, v16 offset:43584
	v_mul_f32_e32 v20, v148, v20
	v_or_b32_e32 v46, v42, v50
	v_lshl_add_u32 v16, v46, 2, v28
	ds_write_b32 v16, v20
	v_add_f32_e32 v16, v45, v17
	v_mul_f32_e32 v16, 0xbfb8aa3b, v16
	v_exp_f32_e32 v16, v16
	v_add_f32_e32 v17, v44, v21
	v_mul_f32_e32 v17, 0xbfb8aa3b, v17
	v_exp_f32_e32 v17, v17
	v_add_f32_e32 v16, 1.0, v16
	v_rcp_f32_e32 v16, v16
	v_add_u32_e32 v21, v39, v51
	v_add_f32_e32 v17, 1.0, v17
	v_rcp_f32_e32 v17, v17
	v_mul_f32_e32 v16, 0xc1000000, v16
	v_mul_f32_e32 v16, v49, v16
	v_mul_f32_e32 v16, 0x3fb8aa3b, v16
	v_exp_f32_e32 v16, v16
	v_lshl_add_u32 v47, v21, 2, v111
	v_fma_f32 v20, -v16, v16, 1.0
	v_max_f32_e32 v20, 0, v20
	v_sqrt_f32_e32 v20, v20
	s_nop 0
	v_mul_f32_e32 v17, v17, v20
	ds_write_b32 v47, v16 offset:43584
	v_mul_f32_e32 v17, v149, v17
	v_or_b32_e32 v20, v39, v50
	v_lshl_add_u32 v16, v20, 2, v28
	ds_write_b32 v16, v17
	v_add_f32_e32 v16, v45, v18
	v_mul_f32_e32 v16, 0xbfb8aa3b, v16
	v_exp_f32_e32 v16, v16
	v_add_f32_e32 v17, v44, v22
	v_mul_f32_e32 v17, 0xbfb8aa3b, v17
	v_exp_f32_e32 v17, v17
	v_add_f32_e32 v16, 1.0, v16
	v_rcp_f32_e32 v16, v16
	v_add_u32_e32 v20, v38, v51
	v_add_f32_e32 v17, 1.0, v17
	v_rcp_f32_e32 v17, v17
	v_mul_f32_e32 v16, 0xc1000000, v16
	v_mul_f32_e32 v16, v49, v16
	v_mul_f32_e32 v16, 0x3fb8aa3b, v16
	v_exp_f32_e32 v16, v16
	v_lshl_add_u32 v46, v20, 2, v111
	v_fma_f32 v18, -v16, v16, 1.0
	v_max_f32_e32 v18, 0, v18
	v_sqrt_f32_e32 v18, v18
	s_nop 0
	v_mul_f32_e32 v17, v17, v18
	ds_write_b32 v46, v16 offset:43584
	v_mul_f32_e32 v17, v150, v17
	v_or_b32_e32 v18, v38, v50
	v_lshl_add_u32 v16, v18, 2, v28
	ds_write_b32 v16, v17
	v_add_f32_e32 v16, v45, v19
	v_mul_f32_e32 v16, 0xbfb8aa3b, v16
	v_exp_f32_e32 v16, v16
	v_add_f32_e32 v17, v44, v23
	v_mul_f32_e32 v17, 0xbfb8aa3b, v17
	v_exp_f32_e32 v17, v17
	v_add_f32_e32 v16, 1.0, v16
	v_rcp_f32_e32 v16, v16
	v_add_u32_e32 v19, v37, v51
	v_add_f32_e32 v17, 1.0, v17
	v_rcp_f32_e32 v17, v17
	v_mul_f32_e32 v16, 0xc1000000, v16
	v_mul_f32_e32 v16, v49, v16
	v_mul_f32_e32 v16, 0x3fb8aa3b, v16
	v_exp_f32_e32 v16, v16
	v_lshl_add_u32 v44, v19, 2, v111
	v_or_b32_e32 v45, 32, v35
	v_mov_b32_e32 v51, v105
	v_fma_f32 v18, -v16, v16, 1.0
	v_max_f32_e32 v18, 0, v18
	v_sqrt_f32_e32 v18, v18
	v_max_f32_e64 v49, -v43, -v43
	v_mul_f32_e64 v43, |v43|, s14
	v_exp_f32_e32 v43, v43
	v_mul_f32_e32 v17, v17, v18
	ds_write_b32 v44, v16 offset:43584
	v_add_f32_e32 v43, 1.0, v43
	v_log_f32_e32 v43, v43
	v_max_f32_e32 v49, 0, v49
	v_mul_f32_e32 v17, v151, v17
	v_or_b32_e32 v18, v37, v50
	v_lshl_add_u32 v16, v18, 2, v28
	v_lshlrev_b32_e32 v50, 7, v45
	ds_write_b32 v16, v17
	v_lshl_add_u64 v[16:17], s[2:3], 0, v[50:51]
	v_lshl_add_u64 v[20:21], v[16:17], 0, v[24:25]
	global_load_dwordx4 v[16:19], v[20:21], off
	s_waitcnt vmcnt(0)
	v_mfma_f32_16x16x32_bf16 v[16:19], v[12:15], v[16:19], 0
	global_load_dwordx4 v[20:23], v[20:21], off offset:64
	v_fmac_f32_e32 v49, 0x3f317218, v43
	v_or_b32_e32 v43, s73, v45
	s_waitcnt vmcnt(0)
	v_mfma_f32_16x16x32_bf16 v[16:19], v[8:11], v[20:23], v[16:19]
	v_lshl_add_u64 v[20:21], s[0:1], 0, v[50:51]
	v_lshl_add_u64 v[50:51], v[20:21], 0, v[24:25]
	global_load_dwordx4 v[20:23], v[50:51], off
	s_nop 4
	v_add_f32_e32 v16, v41, v16
	global_load_dwordx4 v[50:53], v[50:51], off offset:64
	v_mul_f32_e32 v16, 0xbfb8aa3b, v16
	v_exp_f32_e32 v16, v16
	s_waitcnt vmcnt(1)
	v_mfma_f32_16x16x32_bf16 v[20:23], v[12:15], v[20:23], 0
	v_add_f32_e32 v16, 1.0, v16
	v_rcp_f32_e32 v16, v16
	v_or_b32_e32 v35, 48, v35
	s_waitcnt vmcnt(0)
	v_mfma_f32_16x16x32_bf16 v[20:23], v[8:11], v[50:53], v[20:23]
	v_mul_f32_e32 v16, 0xc1000000, v16
	v_mul_f32_e32 v16, v49, v16
	v_mul_f32_e32 v16, 0x3fb8aa3b, v16
	v_exp_f32_e32 v16, v16
	s_nop 3
	v_add_f32_e32 v20, v40, v20
	v_mul_f32_e32 v20, 0xbfb8aa3b, v20
	v_exp_f32_e32 v20, v20
	v_fma_f32 v45, -v16, v16, 1.0
	v_max_f32_e32 v45, 0, v45
	v_sqrt_f32_e32 v45, v45
	v_add_f32_e32 v20, 1.0, v20
	v_rcp_f32_e32 v20, v20
	s_nop 0
	v_mul_f32_e32 v20, v20, v45
	ds_write_b32 v48, v16 offset:43648
	v_mul_f32_e32 v20, v152, v20
	v_or_b32_e32 v45, v42, v43
	v_lshl_add_u32 v16, v45, 2, v28
	ds_write_b32 v16, v20
	v_add_f32_e32 v16, v41, v17
	v_mul_f32_e32 v16, 0xbfb8aa3b, v16
	v_exp_f32_e32 v16, v16
	v_add_f32_e32 v17, v40, v21
	v_mul_f32_e32 v17, 0xbfb8aa3b, v17
	v_exp_f32_e32 v17, v17
	v_add_f32_e32 v16, 1.0, v16
	v_rcp_f32_e32 v16, v16
	v_add_f32_e32 v17, 1.0, v17
	v_rcp_f32_e32 v17, v17
	v_mul_f32_e32 v16, 0xc1000000, v16
	v_mul_f32_e32 v16, v49, v16
	v_mul_f32_e32 v16, 0x3fb8aa3b, v16
	v_exp_f32_e32 v16, v16
	s_nop 0
	v_fma_f32 v20, -v16, v16, 1.0
	v_max_f32_e32 v20, 0, v20
	v_sqrt_f32_e32 v20, v20
	s_nop 0
	v_mul_f32_e32 v17, v17, v20
	ds_write_b32 v47, v16 offset:43648
	v_mul_f32_e32 v17, v153, v17
	v_or_b32_e32 v20, v39, v43
	v_lshl_add_u32 v16, v20, 2, v28
	ds_write_b32 v16, v17
	v_add_f32_e32 v16, v41, v18
	v_mul_f32_e32 v16, 0xbfb8aa3b, v16
	v_exp_f32_e32 v16, v16
	v_add_f32_e32 v17, v40, v22
	v_mul_f32_e32 v17, 0xbfb8aa3b, v17
	v_exp_f32_e32 v17, v17
	v_add_f32_e32 v16, 1.0, v16
	v_rcp_f32_e32 v16, v16
	v_add_f32_e32 v17, 1.0, v17
	v_rcp_f32_e32 v17, v17
	v_mul_f32_e32 v16, 0xc1000000, v16
	v_mul_f32_e32 v16, v49, v16
	v_mul_f32_e32 v16, 0x3fb8aa3b, v16
	v_exp_f32_e32 v16, v16
	s_nop 0
	v_fma_f32 v18, -v16, v16, 1.0
	v_max_f32_e32 v18, 0, v18
	v_sqrt_f32_e32 v18, v18
	s_nop 0
	v_mul_f32_e32 v17, v17, v18
	ds_write_b32 v46, v16 offset:43648
	v_mul_f32_e32 v17, v154, v17
	v_or_b32_e32 v18, v38, v43
	v_lshl_add_u32 v16, v18, 2, v28
	ds_write_b32 v16, v17
	v_add_f32_e32 v16, v41, v19
	v_mul_f32_e32 v16, 0xbfb8aa3b, v16
	v_exp_f32_e32 v16, v16
	v_add_f32_e32 v17, v40, v23
	v_mul_f32_e32 v17, 0xbfb8aa3b, v17
	v_exp_f32_e32 v17, v17
	v_add_f32_e32 v16, 1.0, v16
	v_rcp_f32_e32 v16, v16
	v_lshlrev_b32_e32 v40, 7, v35
	v_add_f32_e32 v17, 1.0, v17
	v_rcp_f32_e32 v17, v17
	v_mul_f32_e32 v16, 0xc1000000, v16
	v_mul_f32_e32 v16, v49, v16
	v_mul_f32_e32 v16, 0x3fb8aa3b, v16
	v_exp_f32_e32 v16, v16
	v_mov_b32_e32 v41, v105
	v_fma_f32 v18, -v16, v16, 1.0
	v_max_f32_e32 v18, 0, v18
	v_sqrt_f32_e32 v18, v18
	s_nop 0
	v_mul_f32_e32 v17, v17, v18
	ds_write_b32 v44, v16 offset:43648
	v_mul_f32_e32 v17, v155, v17
	v_or_b32_e32 v18, v37, v43
	v_lshl_add_u32 v16, v18, 2, v28
	ds_write_b32 v16, v17
	v_lshl_add_u64 v[16:17], s[2:3], 0, v[40:41]
	v_lshl_add_u64 v[20:21], v[16:17], 0, v[24:25]
	global_load_dwordx4 v[16:19], v[20:21], off
	s_waitcnt vmcnt(0)
	v_mfma_f32_16x16x32_bf16 v[16:19], v[12:15], v[16:19], 0
	global_load_dwordx4 v[20:23], v[20:21], off offset:64
	s_waitcnt vmcnt(0)
	v_mfma_f32_16x16x32_bf16 v[16:19], v[8:11], v[20:23], v[16:19]
	v_lshl_add_u64 v[20:21], s[0:1], 0, v[40:41]
	v_lshl_add_u64 v[24:25], v[20:21], 0, v[24:25]
	global_load_dwordx4 v[20:23], v[24:25], off
	s_waitcnt vmcnt(0)
	v_mfma_f32_16x16x32_bf16 v[12:15], v[12:15], v[20:23], 0
	global_load_dwordx4 v[20:23], v[24:25], off offset:64
	s_waitcnt vmcnt(0)
	v_mfma_f32_16x16x32_bf16 v[8:11], v[8:11], v[20:23], v[12:15]
	s_nop 4
	v_add_f32_e32 v14, v33, v16
	v_mul_f32_e64 v13, |v34|, s14
	v_mul_f32_e32 v14, 0xbfb8aa3b, v14
	v_exp_f32_e32 v13, v13
	v_exp_f32_e32 v14, v14
	v_max_f32_e64 v12, -v34, -v34
	v_max_f32_e32 v12, 0, v12
	v_add_f32_e32 v13, 1.0, v13
	v_add_f32_e32 v14, 1.0, v14
	v_log_f32_e32 v13, v13
	v_rcp_f32_e32 v14, v14
	v_add_f32_e32 v8, v32, v8
	v_mul_f32_e32 v8, 0xbfb8aa3b, v8
	v_fmac_f32_e32 v12, 0x3f317218, v13
	v_mul_f32_e32 v14, 0xc1000000, v14
	v_mul_f32_e32 v14, v12, v14
	v_mul_f32_e32 v14, 0x3fb8aa3b, v14
	v_exp_f32_e32 v14, v14
	v_exp_f32_e32 v8, v8
	v_or_b32_e32 v13, s73, v35
	v_add_f32_e32 v9, v32, v9
	v_fma_f32 v15, -v14, v14, 1.0
	v_add_f32_e32 v8, 1.0, v8
	v_max_f32_e32 v15, 0, v15
	v_rcp_f32_e32 v8, v8
	v_sqrt_f32_e32 v15, v15
	v_mul_f32_e32 v9, 0xbfb8aa3b, v9
	v_exp_f32_e32 v9, v9
	v_mul_f32_e32 v8, v8, v15
	ds_write_b32 v48, v14 offset:43712
	v_add_f32_e32 v9, 1.0, v9
	v_rcp_f32_e32 v9, v9
	v_mul_f32_e32 v8, v156, v8
	v_or_b32_e32 v15, v42, v13
	v_lshl_add_u32 v14, v15, 2, v28
	ds_write_b32 v14, v8
	v_add_f32_e32 v8, v33, v17
	v_mul_f32_e32 v8, 0xbfb8aa3b, v8
	v_exp_f32_e32 v8, v8
	s_nop 0
	v_add_f32_e32 v8, 1.0, v8
	v_rcp_f32_e32 v8, v8
	s_nop 0
	v_mul_f32_e32 v8, 0xc1000000, v8
	v_mul_f32_e32 v8, v12, v8
	v_mul_f32_e32 v8, 0x3fb8aa3b, v8
	v_exp_f32_e32 v8, v8
	s_nop 0
	v_fma_f32 v14, -v8, v8, 1.0
	v_max_f32_e32 v14, 0, v14
	v_sqrt_f32_e32 v14, v14
	s_nop 0
	v_mul_f32_e32 v9, v9, v14
	ds_write_b32 v47, v8 offset:43712
	v_mul_f32_e32 v9, v157, v9
	v_or_b32_e32 v14, v39, v13
	v_lshl_add_u32 v8, v14, 2, v28
	ds_write_b32 v8, v9
	v_add_f32_e32 v8, v33, v18
	v_mul_f32_e32 v8, 0xbfb8aa3b, v8
	v_exp_f32_e32 v8, v8
	v_add_f32_e32 v9, v32, v10
	v_mul_f32_e32 v9, 0xbfb8aa3b, v9
	v_exp_f32_e32 v9, v9
	v_add_f32_e32 v8, 1.0, v8
	v_rcp_f32_e32 v8, v8
	v_add_f32_e32 v9, 1.0, v9
	v_rcp_f32_e32 v9, v9
	v_mul_f32_e32 v8, 0xc1000000, v8
	v_mul_f32_e32 v8, v12, v8
	v_mul_f32_e32 v8, 0x3fb8aa3b, v8
	v_exp_f32_e32 v8, v8
	s_nop 0
	v_fma_f32 v10, -v8, v8, 1.0
	v_max_f32_e32 v10, 0, v10
	v_sqrt_f32_e32 v10, v10
	s_nop 0
	v_mul_f32_e32 v9, v9, v10
	ds_write_b32 v46, v8 offset:43712
	v_mul_f32_e32 v9, v158, v9
	v_or_b32_e32 v10, v38, v13
	v_lshl_add_u32 v8, v10, 2, v28
	ds_write_b32 v8, v9
	v_add_f32_e32 v8, v33, v19
	v_mul_f32_e32 v8, 0xbfb8aa3b, v8
	v_exp_f32_e32 v8, v8
	v_add_f32_e32 v9, v32, v11
	v_mul_f32_e32 v9, 0xbfb8aa3b, v9
	v_exp_f32_e32 v9, v9
	v_add_f32_e32 v8, 1.0, v8
	v_rcp_f32_e32 v8, v8
	v_add_f32_e32 v9, 1.0, v9
	v_rcp_f32_e32 v9, v9
	v_mul_f32_e32 v8, 0xc1000000, v8
	v_mul_f32_e32 v8, v12, v8
	v_mul_f32_e32 v8, 0x3fb8aa3b, v8
	v_exp_f32_e32 v8, v8
	v_ashrrev_i32_e32 v12, 8, v30
	v_fma_f32 v10, -v8, v8, 1.0
	v_max_f32_e32 v10, 0, v10
	v_sqrt_f32_e32 v10, v10
	s_nop 0
	v_mul_f32_e32 v9, v9, v10
	ds_write_b32 v44, v8 offset:43712
	v_mul_f32_e32 v9, v159, v9
	v_or_b32_e32 v10, v37, v13
	v_lshl_add_u32 v8, v10, 2, v28
	ds_write_b32 v8, v9
	v_bfe_u32 v8, v30, 6, 2
	v_lshlrev_b32_e32 v9, 4, v8
	v_xor_b32_e32 v10, 63, v9
	v_cndmask_b32_e32 v25, v10, v9, vcc
	v_lshl_or_b32 v10, v12, 14, v104
	v_lshl_or_b32 v11, v25, 8, v10
	s_waitcnt lgkmcnt(0)
	s_barrier
	v_add_u32_e32 v13, v111, v11
	v_add_u32_e32 v11, v28, v11
	ds_read_b32 v17, v13 offset:43520
	ds_read_b32 v22, v11
	v_or_b32_e32 v11, 1, v9
	v_xor_b32_e32 v177, 62, v9
	v_cndmask_b32_e32 v19, v177, v11, vcc
	v_lshl_or_b32 v11, v19, 8, v10
	v_add_u32_e32 v179, v111, v11
	v_add_u32_e32 v11, v28, v11
	ds_read_b32 v15, v11
	ds_read_b32 v161, v179 offset:43520
	v_or_b32_e32 v11, 2, v9
	v_xor_b32_e32 v176, 61, v9
	v_cndmask_b32_e32 v20, v176, v11, vcc
	v_lshl_or_b32 v11, v20, 8, v10
	v_add_u32_e32 v178, v111, v11
	v_add_u32_e32 v11, v28, v11
	ds_read_b32 v16, v11
	ds_read_b32 v162, v178 offset:43520
	v_or_b32_e32 v11, 3, v9
	v_xor_b32_e32 v177, 60, v9
	v_cndmask_b32_e32 v21, v177, v11, vcc
	v_lshl_or_b32 v11, v21, 8, v10
	v_add_u32_e32 v179, v111, v11
	v_add_u32_e32 v11, v28, v11
	ds_read_b32 v18, v11
	ds_read_b32 v163, v179 offset:43520
	v_or_b32_e32 v11, 4, v9
	v_xor_b32_e32 v176, 59, v9
	v_cndmask_b32_e32 v36, v176, v11, vcc
	v_lshl_or_b32 v11, v36, 8, v10
	v_add_u32_e32 v178, v111, v11
	v_add_u32_e32 v11, v28, v11
	ds_read_b32 v33, v11
	ds_read_b32 v164, v178 offset:43520
	v_or_b32_e32 v11, 5, v9
	v_xor_b32_e32 v177, 58, v9
	v_cndmask_b32_e32 v37, v177, v11, vcc
	v_lshl_or_b32 v11, v37, 8, v10
	v_add_u32_e32 v179, v111, v11
	v_add_u32_e32 v11, v28, v11
	ds_read_b32 v34, v11
	ds_read_b32 v165, v179 offset:43520
	v_or_b32_e32 v11, 6, v9
	v_xor_b32_e32 v176, 57, v9
	v_cndmask_b32_e32 v39, v176, v11, vcc
	v_lshl_or_b32 v11, v39, 8, v10
	v_add_u32_e32 v178, v111, v11
	v_add_u32_e32 v11, v28, v11
	ds_read_b32 v35, v11
	ds_read_b32 v166, v178 offset:43520
	v_or_b32_e32 v11, 7, v9
	v_xor_b32_e32 v177, 56, v9
	v_cndmask_b32_e32 v45, v177, v11, vcc
	v_lshl_or_b32 v11, v45, 8, v10
	v_add_u32_e32 v179, v111, v11
	v_add_u32_e32 v11, v28, v11
	ds_read_b32 v42, v11
	ds_read_b32 v167, v179 offset:43520
	v_or_b32_e32 v11, 8, v9
	v_xor_b32_e32 v176, 55, v9
	v_cndmask_b32_e32 v46, v176, v11, vcc
	v_lshl_or_b32 v11, v46, 8, v10
	v_add_u32_e32 v178, v111, v11
	v_add_u32_e32 v11, v28, v11
	ds_read_b32 v43, v11
	ds_read_b32 v168, v178 offset:43520
	v_or_b32_e32 v11, 9, v9
	v_xor_b32_e32 v177, 54, v9
	v_cndmask_b32_e32 v48, v177, v11, vcc
	v_lshl_or_b32 v11, v48, 8, v10
	v_add_u32_e32 v179, v111, v11
	v_add_u32_e32 v11, v28, v11
	ds_read_b32 v44, v11
	ds_read_b32 v169, v179 offset:43520
	v_or_b32_e32 v11, 10, v9
	v_xor_b32_e32 v176, 53, v9
	v_cndmask_b32_e32 v54, v176, v11, vcc
	v_lshl_or_b32 v11, v54, 8, v10
	v_add_u32_e32 v178, v111, v11
	v_add_u32_e32 v11, v28, v11
	ds_read_b32 v51, v11
	ds_read_b32 v170, v178 offset:43520
	v_or_b32_e32 v11, 11, v9
	v_xor_b32_e32 v177, 52, v9
	v_cndmask_b32_e32 v55, v177, v11, vcc
	v_lshl_or_b32 v11, v55, 8, v10
	v_add_u32_e32 v179, v111, v11
	v_add_u32_e32 v11, v28, v11
	ds_read_b32 v52, v11
	ds_read_b32 v171, v179 offset:43520
	v_or_b32_e32 v11, 12, v9
	v_xor_b32_e32 v176, 51, v9
	v_cndmask_b32_e32 v57, v176, v11, vcc
	v_lshl_or_b32 v11, v57, 8, v10
	v_add_u32_e32 v178, v111, v11
	v_add_u32_e32 v11, v28, v11
	ds_read_b32 v53, v11
	ds_read_b32 v172, v178 offset:43520
	v_or_b32_e32 v11, 13, v9
	v_xor_b32_e32 v177, 50, v9
	v_cndmask_b32_e32 v62, v177, v11, vcc
	v_lshl_or_b32 v11, v62, 8, v10
	v_add_u32_e32 v179, v111, v11
	v_add_u32_e32 v11, v28, v11
	ds_read_b32 v60, v11
	ds_read_b32 v173, v179 offset:43520
	v_or_b32_e32 v11, 14, v9
	v_xor_b32_e32 v176, 49, v9
	v_cndmask_b32_e32 v63, v176, v11, vcc
	v_lshl_or_b32 v11, v63, 8, v10
	v_add_u32_e32 v178, v111, v11
	v_add_u32_e32 v11, v28, v11
	ds_read_b32 v61, v11
	ds_read_b32 v174, v178 offset:43520
	v_or_b32_e32 v11, 15, v9
	v_xor_b32_e32 v177, 48, v9
	v_cndmask_b32_e32 v65, v177, v11, vcc
	v_lshl_or_b32 v11, v65, 8, v10
	v_add_u32_e32 v179, v111, v11
	v_add_u32_e32 v11, v28, v11
	ds_read_b32 v32, v11
	ds_read_b32 v175, v179 offset:43520
	v_and_b32_e32 v9, 0x3fffff00, v30
	v_lshlrev_b32_e32 v10, 6, v8
	v_cmp_ne_u32_e32 vcc, 0, v8
	v_or3_b32 v9, v10, v9, v31
	s_waitcnt lgkmcnt(0)
	v_fmac_f32_e32 v22, 0, v17
	v_fmac_f32_e32 v15, v22, v161
	v_mul_f32_e32 v13, v17, v161
	v_fmac_f32_e32 v16, v15, v162
	v_mul_f32_e32 v14, v13, v162
	v_fmac_f32_e32 v18, v16, v163
	v_mul_f32_e32 v38, v14, v163
	v_fmac_f32_e32 v33, v18, v164
	v_mul_f32_e32 v23, v38, v164
	v_fmac_f32_e32 v34, v33, v165
	v_mul_f32_e32 v24, v23, v165
	v_fmac_f32_e32 v35, v34, v166
	v_mul_f32_e32 v47, v24, v166
	v_fmac_f32_e32 v42, v35, v167
	v_mul_f32_e32 v40, v47, v167
	v_fmac_f32_e32 v43, v42, v168
	v_mul_f32_e32 v41, v40, v168
	v_fmac_f32_e32 v44, v43, v169
	v_mul_f32_e32 v56, v41, v169
	v_fmac_f32_e32 v51, v44, v170
	v_mul_f32_e32 v49, v56, v170
	v_fmac_f32_e32 v52, v51, v171
	v_mul_f32_e32 v50, v49, v171
	v_fmac_f32_e32 v53, v52, v172
	v_mul_f32_e32 v64, v50, v172
	v_fmac_f32_e32 v60, v53, v173
	v_mul_f32_e32 v58, v64, v173
	v_fmac_f32_e32 v61, v60, v174
	v_mul_f32_e32 v59, v58, v174
	v_fmac_f32_e32 v32, v61, v175
	v_mul_f32_e32 v66, v59, v175
	v_lshlrev_b32_e32 v9, 2, v9
	v_add_u32_e32 v10, v27, v9
	v_add_u32_e32 v9, v29, v9
	ds_write_b32 v10, v66
	ds_write_b32 v9, v32
	s_waitcnt lgkmcnt(0)
	s_barrier
	s_and_saveexec_b64 s[0:1], vcc
	s_cbranch_execz .LBB0_372
	v_lshlrev_b32_e32 v9, 2, v30
	v_and_b32_e32 v9, 0xfffffcfc, v9
	v_add_u32_e32 v10, v29, v9
	v_add_u32_e32 v9, v27, v9
	ds_read_b32 v67, v9
	ds_read_b32 v68, v10
	s_waitcnt lgkmcnt(0)
	v_fmac_f32_e32 v68, 0, v67
